# speedup vs baseline: 1.0015x; 1.0015x over previous
.LBB1_14:
	v_add_u32_e32 v118, s4, v224
	ds_read_b128 v[66:69], v118
	ds_read_b128 v[98:101], v218 offset:8192
	ds_read_b128 v[102:105], v118 offset:32
	ds_read_b128 v[82:85], v118 offset:384
	ds_read_b128 v[86:89], v118 offset:416
	ds_read_b128 v[90:93], v118 offset:448
	ds_read_b128 v[94:97], v118 offset:480
	s_waitcnt lgkmcnt(6)
	v_pk_add_f16 v66, v142, v66
	v_pk_add_f16 v67, v143, v67
	v_pk_add_f16 v68, v144, v68
	v_pk_add_f16 v69, v145, v69
	v_or_b32_e32 v71, 0x80008000, v68
	v_or_b32_e32 v70, 0x80008000, v69
	v_or_b32_e32 v72, 0x80008000, v67
	v_or_b32_e32 v73, 0x80008000, v66
	v_pk_fma_f16 v74, v73, s3, v221 op_sel_hi:[1,0,0]
	v_pk_fma_f16 v75, v72, s3, v221 op_sel_hi:[1,0,0]
	v_pk_fma_f16 v76, v71, s3, v221 op_sel_hi:[1,0,0]
	v_pk_fma_f16 v77, v70, s3, v221 op_sel_hi:[1,0,0]
	v_pk_fma_f16 v76, v76, v71, s20 op_sel_hi:[1,1,0]
	v_pk_fma_f16 v77, v77, v70, s20 op_sel_hi:[1,1,0]
	v_pk_fma_f16 v75, v75, v72, s20 op_sel_hi:[1,1,0]
	v_pk_fma_f16 v74, v74, v73, s20 op_sel_hi:[1,1,0]
	v_pk_fma_f16 v75, v75, v72, s21 op_sel_hi:[1,1,0]
	v_pk_fma_f16 v74, v74, v73, s21 op_sel_hi:[1,1,0]
	v_pk_fma_f16 v76, v76, v71, s21 op_sel_hi:[1,1,0]
	v_pk_fma_f16 v77, v77, v70, s21 op_sel_hi:[1,1,0]
	v_pk_max_f16 v66, v66, 0
	v_exp_f16_e32 v78, v74
	v_exp_f16_e32 v79, v75
	v_exp_f16_e32 v80, v76
	v_exp_f16_e32 v81, v77
	v_exp_f16_sdwa v78, v74 dst_sel:WORD_1 dst_unused:UNUSED_PRESERVE src0_sel:WORD_1
	v_exp_f16_sdwa v79, v75 dst_sel:WORD_1 dst_unused:UNUSED_PRESERVE src0_sel:WORD_1
	v_exp_f16_sdwa v80, v76 dst_sel:WORD_1 dst_unused:UNUSED_PRESERVE src0_sel:WORD_1
	v_exp_f16_sdwa v81, v77 dst_sel:WORD_1 dst_unused:UNUSED_PRESERVE src0_sel:WORD_1
	v_pk_max_f16 v67, v67, 0
	v_pk_max_f16 v68, v68, 0
	v_pk_max_f16 v69, v69, 0
	v_pk_fma_f16 v108, v71, v80, v68
	v_pk_fma_f16 v109, v70, v81, v69
	v_pk_fma_f16 v107, v72, v79, v67
	v_pk_fma_f16 v106, v73, v78, v66
	ds_read_b128 v[66:69], v118 offset:512
	ds_read_b128 v[70:73], v118 offset:544
	ds_read_b128 v[74:77], v118 offset:576
	ds_read_b128 v[78:81], v118 offset:608
	ds_read_b128 v[110:113], v218 offset:9216
	s_setprio 2
	s_waitcnt lgkmcnt(5)
	v_mfma_f32_32x32x16_f16 v[82:97], v[150:153], v[106:109], v[82:97]
	s_waitcnt lgkmcnt(1)
	v_mfma_f32_32x32x16_f16 v[66:81], v[98:101], v[106:109], v[66:81]
	s_setprio 1
	v_pk_add_f16 v98, v146, v102
	v_pk_add_f16 v99, v147, v103
	v_pk_add_f16 v100, v148, v104
	v_pk_add_f16 v101, v149, v105
	v_or_b32_e32 v103, 0x80008000, v100
	v_or_b32_e32 v102, 0x80008000, v101
	v_or_b32_e32 v104, 0x80008000, v99
	v_or_b32_e32 v105, 0x80008000, v98
	v_pk_fma_f16 v106, v105, s3, v221 op_sel_hi:[1,0,0]
	v_pk_fma_f16 v107, v104, s3, v221 op_sel_hi:[1,0,0]
	v_pk_fma_f16 v108, v103, s3, v221 op_sel_hi:[1,0,0]
	v_pk_fma_f16 v109, v102, s3, v221 op_sel_hi:[1,0,0]
	v_pk_fma_f16 v108, v108, v103, s20 op_sel_hi:[1,1,0]
	v_pk_fma_f16 v109, v109, v102, s20 op_sel_hi:[1,1,0]
	v_pk_fma_f16 v107, v107, v104, s20 op_sel_hi:[1,1,0]
	v_pk_fma_f16 v106, v106, v105, s20 op_sel_hi:[1,1,0]
	v_pk_fma_f16 v107, v107, v104, s21 op_sel_hi:[1,1,0]
	v_pk_fma_f16 v106, v106, v105, s21 op_sel_hi:[1,1,0]
	v_pk_fma_f16 v108, v108, v103, s21 op_sel_hi:[1,1,0]
	v_pk_fma_f16 v109, v109, v102, s21 op_sel_hi:[1,1,0]
	v_pk_max_f16 v98, v98, 0
	v_pk_max_f16 v99, v99, 0
	v_pk_max_f16 v100, v100, 0
	v_pk_max_f16 v101, v101, 0
	v_exp_f16_e32 v114, v106
	v_exp_f16_e32 v115, v107
	v_exp_f16_e32 v116, v108
	v_exp_f16_e32 v117, v109
	v_exp_f16_sdwa v114, v106 dst_sel:WORD_1 dst_unused:UNUSED_PRESERVE src0_sel:WORD_1
	v_exp_f16_sdwa v115, v107 dst_sel:WORD_1 dst_unused:UNUSED_PRESERVE src0_sel:WORD_1
	v_exp_f16_sdwa v116, v108 dst_sel:WORD_1 dst_unused:UNUSED_PRESERVE src0_sel:WORD_1
	v_exp_f16_sdwa v117, v109 dst_sel:WORD_1 dst_unused:UNUSED_PRESERVE src0_sel:WORD_1
	s_nop 0
	v_pk_fma_f16 v101, v102, v117, v101
	v_pk_fma_f16 v100, v103, v116, v100
	v_pk_fma_f16 v99, v104, v115, v99
	v_pk_fma_f16 v98, v105, v114, v98
	ds_read_b128 v[102:105], v118 offset:64
	ds_read_b128 v[106:109], v218 offset:2048
	s_setprio 2
	v_mfma_f32_32x32x16_f16 v[82:97], v[154:157], v[98:101], v[82:97]
	v_add_u32_e32 v225, s4, v223
	ds_read_b128 v[126:129], v225
	ds_read_b128 v[130:133], v225 offset:16
	ds_read_b128 v[134:137], v225 offset:32
	ds_read_b128 v[138:141], v225 offset:48
	ds_read_b128 v[150:153], v218 offset:19456
	ds_read_b128 v[154:157], v218 offset:20480
	s_waitcnt lgkmcnt(7)
	v_pk_add_f16 v102, v158, v102
	v_pk_add_f16 v103, v159, v103
	v_pk_add_f16 v104, v160, v104
	v_pk_add_f16 v105, v161, v105
	v_mfma_f32_32x32x16_f16 v[66:81], v[110:113], v[98:101], v[66:81]
	s_setprio 1
	v_or_b32_e32 v110, 0x80008000, v105
	v_or_b32_e32 v111, 0x80008000, v104
	v_or_b32_e32 v112, 0x80008000, v103
	v_or_b32_e32 v113, 0x80008000, v102
	v_pk_fma_f16 v114, v113, s3, v221 op_sel_hi:[1,0,0]
	v_pk_fma_f16 v115, v112, s3, v221 op_sel_hi:[1,0,0]
	v_pk_fma_f16 v116, v111, s3, v221 op_sel_hi:[1,0,0]
	v_pk_fma_f16 v117, v110, s3, v221 op_sel_hi:[1,0,0]
	ds_read_b128 v[98:101], v118 offset:96
	v_pk_fma_f16 v117, v117, v110, s20 op_sel_hi:[1,1,0]
	v_pk_fma_f16 v116, v116, v111, s20 op_sel_hi:[1,1,0]
	v_pk_fma_f16 v115, v115, v112, s20 op_sel_hi:[1,1,0]
	v_pk_fma_f16 v114, v114, v113, s20 op_sel_hi:[1,1,0]
	v_pk_max_f16 v102, v102, 0
	v_pk_max_f16 v103, v103, 0
	v_pk_max_f16 v104, v104, 0
	v_pk_max_f16 v105, v105, 0
	v_pk_fma_f16 v114, v114, v113, s21 op_sel_hi:[1,1,0]
	v_pk_fma_f16 v115, v115, v112, s21 op_sel_hi:[1,1,0]
	v_pk_fma_f16 v116, v116, v111, s21 op_sel_hi:[1,1,0]
	v_pk_fma_f16 v117, v117, v110, s21 op_sel_hi:[1,1,0]
	s_nop 0
	v_exp_f16_e32 v119, v114
	v_exp_f16_e32 v120, v115
	v_exp_f16_e32 v121, v116
	v_exp_f16_e32 v122, v117
	v_exp_f16_sdwa v119, v114 dst_sel:WORD_1 dst_unused:UNUSED_PRESERVE src0_sel:WORD_1
	v_exp_f16_sdwa v120, v115 dst_sel:WORD_1 dst_unused:UNUSED_PRESERVE src0_sel:WORD_1
	v_exp_f16_sdwa v121, v116 dst_sel:WORD_1 dst_unused:UNUSED_PRESERVE src0_sel:WORD_1
	v_exp_f16_sdwa v122, v117 dst_sel:WORD_1 dst_unused:UNUSED_PRESERVE src0_sel:WORD_1
	s_nop 0
	v_pk_fma_f16 v105, v110, v122, v105
	v_pk_fma_f16 v104, v111, v121, v104
	v_pk_fma_f16 v103, v112, v120, v103
	v_pk_fma_f16 v102, v113, v119, v102
	ds_read_b128 v[110:113], v218 offset:3072
	s_waitcnt lgkmcnt(1)
	v_pk_add_f16 v98, v162, v98
	s_setprio 2
	v_mfma_f32_32x32x16_f16 v[82:97], v[106:109], v[102:105], v[82:97]
	ds_read_b128 v[106:109], v218 offset:10240
	ds_read_b128 v[114:117], v218 offset:11264
	v_pk_add_f16 v99, v163, v99
	v_pk_add_f16 v100, v164, v100
	v_pk_add_f16 v101, v165, v101
	s_waitcnt lgkmcnt(1)
	v_mfma_f32_32x32x16_f16 v[66:81], v[106:109], v[102:105], v[66:81]
	s_setprio 0
	v_or_b32_e32 v102, 0x80008000, v101
	v_or_b32_e32 v103, 0x80008000, v100
	v_or_b32_e32 v104, 0x80008000, v99
	v_or_b32_e32 v105, 0x80008000, v98
	v_pk_fma_f16 v106, v105, s3, v221 op_sel_hi:[1,0,0]
	v_pk_fma_f16 v107, v104, s3, v221 op_sel_hi:[1,0,0]
	v_pk_fma_f16 v108, v103, s3, v221 op_sel_hi:[1,0,0]
	v_pk_fma_f16 v109, v102, s3, v221 op_sel_hi:[1,0,0]
	v_pk_fma_f16 v108, v108, v103, s20 op_sel_hi:[1,1,0]
	v_pk_fma_f16 v109, v109, v102, s20 op_sel_hi:[1,1,0]
	v_pk_fma_f16 v107, v107, v104, s20 op_sel_hi:[1,1,0]
	v_pk_fma_f16 v106, v106, v105, s20 op_sel_hi:[1,1,0]
	v_pk_fma_f16 v107, v107, v104, s21 op_sel_hi:[1,1,0]
	v_pk_fma_f16 v106, v106, v105, s21 op_sel_hi:[1,1,0]
	v_pk_fma_f16 v108, v108, v103, s21 op_sel_hi:[1,1,0]
	v_pk_fma_f16 v109, v109, v102, s21 op_sel_hi:[1,1,0]
	v_pk_max_f16 v98, v98, 0
	v_pk_max_f16 v99, v99, 0
	v_pk_max_f16 v100, v100, 0
	v_pk_max_f16 v101, v101, 0
	v_exp_f16_e32 v119, v106
	v_exp_f16_e32 v120, v107
	v_exp_f16_e32 v121, v108
	v_exp_f16_e32 v122, v109
	v_exp_f16_sdwa v119, v106 dst_sel:WORD_1 dst_unused:UNUSED_PRESERVE src0_sel:WORD_1
	v_exp_f16_sdwa v120, v107 dst_sel:WORD_1 dst_unused:UNUSED_PRESERVE src0_sel:WORD_1
	v_exp_f16_sdwa v121, v108 dst_sel:WORD_1 dst_unused:UNUSED_PRESERVE src0_sel:WORD_1
	v_exp_f16_sdwa v122, v109 dst_sel:WORD_1 dst_unused:UNUSED_PRESERVE src0_sel:WORD_1
	s_nop 0
	v_pk_fma_f16 v101, v102, v122, v101
	v_pk_fma_f16 v100, v103, v121, v100
	v_pk_fma_f16 v99, v104, v120, v99
	v_pk_fma_f16 v98, v105, v119, v98
	ds_read_b128 v[102:105], v118 offset:128
	ds_read_b128 v[106:109], v218 offset:4096
	s_setprio 2
	v_mfma_f32_32x32x16_f16 v[82:97], v[110:113], v[98:101], v[82:97]
	s_waitcnt lgkmcnt(1)
	v_pk_add_f16 v102, v166, v102
	v_pk_add_f16 v103, v167, v103
	v_pk_add_f16 v104, v168, v104
	v_pk_add_f16 v105, v169, v105
	v_or_b32_e32 v111, 0x80008000, v104
	v_mfma_f32_32x32x16_f16 v[66:81], v[114:117], v[98:101], v[66:81]
	s_setprio 0
	ds_read_b128 v[226:229], v222
	ds_read_b128 v[230:233], v222 offset:1024
	ds_read_b128 v[234:237], v222 offset:2048
	ds_read_b128 v[238:241], v222 offset:3072
	v_or_b32_e32 v110, 0x80008000, v105
	v_or_b32_e32 v112, 0x80008000, v103
	v_or_b32_e32 v113, 0x80008000, v102
	v_pk_fma_f16 v114, v113, s3, v221 op_sel_hi:[1,0,0]
	v_pk_fma_f16 v115, v112, s3, v221 op_sel_hi:[1,0,0]
	v_pk_fma_f16 v116, v111, s3, v221 op_sel_hi:[1,0,0]
	v_pk_fma_f16 v117, v110, s3, v221 op_sel_hi:[1,0,0]
	ds_read_b128 v[98:101], v118 offset:160
	v_pk_fma_f16 v117, v117, v110, s20 op_sel_hi:[1,1,0]
	v_pk_fma_f16 v116, v116, v111, s20 op_sel_hi:[1,1,0]
	v_pk_fma_f16 v115, v115, v112, s20 op_sel_hi:[1,1,0]
	v_pk_fma_f16 v114, v114, v113, s20 op_sel_hi:[1,1,0]
	v_pk_max_f16 v102, v102, 0
	v_pk_max_f16 v103, v103, 0
	v_pk_max_f16 v104, v104, 0
	v_pk_max_f16 v105, v105, 0
	v_pk_fma_f16 v114, v114, v113, s21 op_sel_hi:[1,1,0]
	v_pk_fma_f16 v115, v115, v112, s21 op_sel_hi:[1,1,0]
	v_pk_fma_f16 v116, v116, v111, s21 op_sel_hi:[1,1,0]
	v_pk_fma_f16 v117, v117, v110, s21 op_sel_hi:[1,1,0]
	s_nop 0
	v_exp_f16_e32 v119, v114
	v_exp_f16_e32 v120, v115
	v_exp_f16_e32 v121, v116
	v_exp_f16_e32 v122, v117
	v_exp_f16_sdwa v119, v114 dst_sel:WORD_1 dst_unused:UNUSED_PRESERVE src0_sel:WORD_1
	v_exp_f16_sdwa v120, v115 dst_sel:WORD_1 dst_unused:UNUSED_PRESERVE src0_sel:WORD_1
	v_exp_f16_sdwa v121, v116 dst_sel:WORD_1 dst_unused:UNUSED_PRESERVE src0_sel:WORD_1
	v_exp_f16_sdwa v122, v117 dst_sel:WORD_1 dst_unused:UNUSED_PRESERVE src0_sel:WORD_1
	s_nop 0
	v_pk_fma_f16 v105, v110, v122, v105
	v_pk_fma_f16 v104, v111, v121, v104
	v_pk_fma_f16 v103, v112, v120, v103
	v_pk_fma_f16 v102, v113, v119, v102
	ds_read_b128 v[110:113], v218 offset:5120
	s_waitcnt lgkmcnt(1)
	v_pk_add_f16 v98, v170, v98
	s_setprio 2
	v_mfma_f32_32x32x16_f16 v[82:97], v[106:109], v[102:105], v[82:97]
	ds_read_b128 v[106:109], v218 offset:12288
	ds_read_b128 v[114:117], v218 offset:13312
	v_pk_add_f16 v99, v171, v99
	v_pk_add_f16 v100, v172, v100
	v_pk_add_f16 v101, v173, v101
	s_waitcnt lgkmcnt(1)
	v_mfma_f32_32x32x16_f16 v[66:81], v[106:109], v[102:105], v[66:81]
	s_setprio 0
	v_or_b32_e32 v102, 0x80008000, v101
	v_or_b32_e32 v103, 0x80008000, v100
	v_or_b32_e32 v104, 0x80008000, v99
	v_or_b32_e32 v105, 0x80008000, v98
	v_pk_fma_f16 v106, v105, s3, v221 op_sel_hi:[1,0,0]
	v_pk_fma_f16 v107, v104, s3, v221 op_sel_hi:[1,0,0]
	v_pk_fma_f16 v108, v103, s3, v221 op_sel_hi:[1,0,0]
	v_pk_fma_f16 v109, v102, s3, v221 op_sel_hi:[1,0,0]
	v_pk_fma_f16 v108, v108, v103, s20 op_sel_hi:[1,1,0]
	v_pk_fma_f16 v109, v109, v102, s20 op_sel_hi:[1,1,0]
	v_pk_fma_f16 v107, v107, v104, s20 op_sel_hi:[1,1,0]
	v_pk_fma_f16 v106, v106, v105, s20 op_sel_hi:[1,1,0]
	v_pk_fma_f16 v107, v107, v104, s21 op_sel_hi:[1,1,0]
	v_pk_fma_f16 v106, v106, v105, s21 op_sel_hi:[1,1,0]
	v_pk_fma_f16 v108, v108, v103, s21 op_sel_hi:[1,1,0]
	v_pk_fma_f16 v109, v109, v102, s21 op_sel_hi:[1,1,0]
	v_pk_max_f16 v98, v98, 0
	v_pk_max_f16 v99, v99, 0
	v_pk_max_f16 v100, v100, 0
	v_pk_max_f16 v101, v101, 0
	v_exp_f16_e32 v119, v106
	v_exp_f16_e32 v120, v107
	v_exp_f16_e32 v121, v108
	v_exp_f16_e32 v122, v109
	v_exp_f16_sdwa v119, v106 dst_sel:WORD_1 dst_unused:UNUSED_PRESERVE src0_sel:WORD_1
	v_exp_f16_sdwa v120, v107 dst_sel:WORD_1 dst_unused:UNUSED_PRESERVE src0_sel:WORD_1
	v_exp_f16_sdwa v121, v108 dst_sel:WORD_1 dst_unused:UNUSED_PRESERVE src0_sel:WORD_1
	v_exp_f16_sdwa v122, v109 dst_sel:WORD_1 dst_unused:UNUSED_PRESERVE src0_sel:WORD_1
	s_nop 0
	v_pk_fma_f16 v101, v102, v122, v101
	v_pk_fma_f16 v100, v103, v121, v100
	v_pk_fma_f16 v99, v104, v120, v99
	v_pk_fma_f16 v98, v105, v119, v98
	ds_read_b128 v[102:105], v118 offset:192
	ds_read_b128 v[106:109], v218 offset:6144
	s_setprio 2
	v_mfma_f32_32x32x16_f16 v[82:97], v[110:113], v[98:101], v[82:97]
	s_waitcnt lgkmcnt(1)
	v_pk_add_f16 v102, v174, v102
	v_pk_add_f16 v103, v175, v103
	v_pk_add_f16 v104, v176, v104
	v_pk_add_f16 v105, v177, v105
	v_or_b32_e32 v111, 0x80008000, v104
	v_mfma_f32_32x32x16_f16 v[66:81], v[114:117], v[98:101], v[66:81]
	s_setprio 0
	v_or_b32_e32 v110, 0x80008000, v105
	v_or_b32_e32 v112, 0x80008000, v103
	v_or_b32_e32 v113, 0x80008000, v102
	v_pk_fma_f16 v114, v113, s3, v221 op_sel_hi:[1,0,0]
	v_pk_fma_f16 v115, v112, s3, v221 op_sel_hi:[1,0,0]
	v_pk_fma_f16 v116, v111, s3, v221 op_sel_hi:[1,0,0]
	v_pk_fma_f16 v117, v110, s3, v221 op_sel_hi:[1,0,0]
	ds_read_b128 v[98:101], v118 offset:224
	v_pk_fma_f16 v117, v117, v110, s20 op_sel_hi:[1,1,0]
	v_pk_fma_f16 v116, v116, v111, s20 op_sel_hi:[1,1,0]
	v_pk_fma_f16 v115, v115, v112, s20 op_sel_hi:[1,1,0]
	v_pk_fma_f16 v114, v114, v113, s20 op_sel_hi:[1,1,0]
	v_pk_max_f16 v102, v102, 0
	v_pk_max_f16 v103, v103, 0
	v_pk_max_f16 v104, v104, 0
	v_pk_max_f16 v105, v105, 0
	v_pk_fma_f16 v114, v114, v113, s21 op_sel_hi:[1,1,0]
	v_pk_fma_f16 v115, v115, v112, s21 op_sel_hi:[1,1,0]
	v_pk_fma_f16 v116, v116, v111, s21 op_sel_hi:[1,1,0]
	v_pk_fma_f16 v117, v117, v110, s21 op_sel_hi:[1,1,0]
	s_waitcnt lgkmcnt(0)
	v_pk_add_f16 v98, v178, v98
	ds_read_b128 v[242:245], v218 offset:16384
	ds_read_b128 v[246:249], v218 offset:17408
	ds_read_b128 v[250:253], v218 offset:18432
	v_exp_f16_e32 v118, v114
	v_exp_f16_e32 v119, v115
	v_exp_f16_e32 v120, v116
	v_exp_f16_e32 v121, v117
	v_exp_f16_sdwa v118, v114 dst_sel:WORD_1 dst_unused:UNUSED_PRESERVE src0_sel:WORD_1
	v_exp_f16_sdwa v119, v115 dst_sel:WORD_1 dst_unused:UNUSED_PRESERVE src0_sel:WORD_1
	v_exp_f16_sdwa v120, v116 dst_sel:WORD_1 dst_unused:UNUSED_PRESERVE src0_sel:WORD_1
	v_exp_f16_sdwa v121, v117 dst_sel:WORD_1 dst_unused:UNUSED_PRESERVE src0_sel:WORD_1
	v_pk_add_f16 v99, v179, v99
	v_pk_fma_f16 v105, v110, v121, v105
	v_pk_fma_f16 v104, v111, v120, v104
	v_pk_fma_f16 v103, v112, v119, v103
	v_pk_fma_f16 v102, v113, v118, v102
	ds_read_b128 v[110:113], v218 offset:7168
	v_pk_add_f16 v100, v180, v100
	s_setprio 2
	v_mfma_f32_32x32x16_f16 v[82:97], v[106:109], v[102:105], v[82:97]
	ds_read_b128 v[106:109], v218 offset:14336
	ds_read_b128 v[114:117], v218 offset:15360
	v_pk_add_f16 v101, v181, v101
	s_waitcnt lgkmcnt(1)
	v_mfma_f32_32x32x16_f16 v[66:81], v[106:109], v[102:105], v[66:81]
	s_setprio 0
	v_or_b32_e32 v102, 0x80008000, v101
	v_or_b32_e32 v103, 0x80008000, v100
	v_or_b32_e32 v104, 0x80008000, v99
	v_or_b32_e32 v105, 0x80008000, v98
	v_pk_fma_f16 v106, v105, s3, v221 op_sel_hi:[1,0,0]
	v_pk_fma_f16 v107, v104, s3, v221 op_sel_hi:[1,0,0]
	v_pk_fma_f16 v108, v103, s3, v221 op_sel_hi:[1,0,0]
	v_pk_fma_f16 v109, v102, s3, v221 op_sel_hi:[1,0,0]
	v_pk_fma_f16 v108, v108, v103, s20 op_sel_hi:[1,1,0]
	v_pk_fma_f16 v109, v109, v102, s20 op_sel_hi:[1,1,0]
	v_pk_fma_f16 v107, v107, v104, s20 op_sel_hi:[1,1,0]
	v_pk_fma_f16 v106, v106, v105, s20 op_sel_hi:[1,1,0]
	v_pk_max_f16 v98, v98, 0
	v_pk_max_f16 v99, v99, 0
	v_pk_max_f16 v100, v100, 0
	v_pk_max_f16 v101, v101, 0
	v_pk_fma_f16 v106, v106, v105, s21 op_sel_hi:[1,1,0]
	v_pk_fma_f16 v107, v107, v104, s21 op_sel_hi:[1,1,0]
	v_pk_fma_f16 v108, v108, v103, s21 op_sel_hi:[1,1,0]
	v_pk_fma_f16 v109, v109, v102, s21 op_sel_hi:[1,1,0]
	s_nop 0
	v_exp_f16_e32 v118, v106
	v_exp_f16_e32 v119, v107
	v_exp_f16_e32 v120, v108
	v_exp_f16_e32 v121, v109
	v_exp_f16_sdwa v118, v106 dst_sel:WORD_1 dst_unused:UNUSED_PRESERVE src0_sel:WORD_1
	v_exp_f16_sdwa v119, v107 dst_sel:WORD_1 dst_unused:UNUSED_PRESERVE src0_sel:WORD_1
	v_exp_f16_sdwa v120, v108 dst_sel:WORD_1 dst_unused:UNUSED_PRESERVE src0_sel:WORD_1
	v_exp_f16_sdwa v121, v109 dst_sel:WORD_1 dst_unused:UNUSED_PRESERVE src0_sel:WORD_1
	s_nop 0
	v_pk_fma_f16 v101, v102, v121, v101
	v_pk_fma_f16 v100, v103, v120, v100
	v_pk_fma_f16 v99, v104, v119, v99
	v_pk_fma_f16 v98, v105, v118, v98
	s_setprio 2
	s_nop 1
	v_mfma_f32_32x32x16_f16 v[82:97], v[110:113], v[98:101], v[82:97]
	s_waitcnt lgkmcnt(0)
	v_mfma_f32_32x32x16_f16 v[66:81], v[114:117], v[98:101], v[66:81]
	s_setprio 2
	ds_read_b128 v[98:101], v222 offset:4096
	ds_read_b128 v[102:105], v222 offset:5120
	ds_read_b128 v[106:109], v222 offset:6144
	ds_read_b128 v[110:113], v222 offset:7168
	s_nop 4
	v_cvt_pk_f16_f32 v114, v82, v83
	v_cvt_pk_f16_f32 v115, v84, v85
	v_cvt_pk_f16_f32 v116, v86, v87
	v_cvt_pk_f16_f32 v117, v88, v89
	v_pk_add_f16 v126, v126, v114
	v_pk_add_f16 v127, v127, v115
	v_pk_add_f16 v128, v128, v116
	v_pk_add_f16 v129, v129, v117
	s_nop 1
	v_mfma_f32_32x32x16_f16 v[226:241], v[242:245], v[126:129], v[226:241]
	ds_read_b128 v[242:245], v218 offset:21504
	v_cvt_pk_f16_f32 v118, v90, v91
	v_cvt_pk_f16_f32 v119, v92, v93
	v_cvt_pk_f16_f32 v120, v94, v95
	v_cvt_pk_f16_f32 v121, v96, v97
	v_pk_add_f16 v130, v130, v118
	v_pk_add_f16 v131, v131, v119
	v_pk_add_f16 v132, v132, v120
	v_pk_add_f16 v133, v133, v121
	s_nop 1
	v_mfma_f32_32x32x16_f16 v[226:241], v[246:249], v[130:133], v[226:241]
	ds_read_b128 v[246:249], v218 offset:22528
	v_cvt_pk_f16_f32 v122, v66, v67
	v_cvt_pk_f16_f32 v123, v68, v69
	v_cvt_pk_f16_f32 v124, v70, v71
	v_cvt_pk_f16_f32 v125, v72, v73
	v_pk_add_f16 v134, v134, v122
	v_pk_add_f16 v135, v135, v123
	v_pk_add_f16 v136, v136, v124
	v_pk_add_f16 v137, v137, v125
	s_nop 1
	v_mfma_f32_32x32x16_f16 v[226:241], v[250:253], v[134:137], v[226:241]
	ds_read_b128 v[250:253], v218 offset:23552
	v_cvt_pk_f16_f32 v182, v74, v75
	v_cvt_pk_f16_f32 v183, v76, v77
	v_cvt_pk_f16_f32 v184, v78, v79
	v_cvt_pk_f16_f32 v185, v80, v81
	v_pk_add_f16 v138, v138, v182
	v_pk_add_f16 v139, v139, v183
	v_pk_add_f16 v140, v140, v184
	v_pk_add_f16 v141, v141, v185
	s_nop 1
	v_mfma_f32_32x32x16_f16 v[226:241], v[150:153], v[138:141], v[226:241]
	ds_read_b128 v[150:153], v218 offset:24576
	ds_read_b128 v[66:69], v222 offset:8192
	ds_read_b128 v[70:73], v222 offset:9216
	ds_read_b128 v[74:77], v222 offset:10240
	ds_read_b128 v[78:81], v222 offset:11264
	ds_read_b128 v[82:85], v222 offset:12288
	ds_read_b128 v[86:89], v222 offset:13312
	ds_read_b128 v[90:93], v222 offset:14336
	ds_read_b128 v[94:97], v222 offset:15360
	s_waitcnt lgkmcnt(12)
	v_mfma_f32_32x32x16_f16 v[98:113], v[154:157], v[126:129], v[98:113]
	ds_read_b128 v[154:157], v218 offset:25600
	s_waitcnt lgkmcnt(12)
	v_mfma_f32_32x32x16_f16 v[98:113], v[242:245], v[130:133], v[98:113]
	ds_read_b128 v[242:245], v218 offset:26624
	s_waitcnt lgkmcnt(12)
	v_mfma_f32_32x32x16_f16 v[98:113], v[246:249], v[134:137], v[98:113]
	ds_read_b128 v[246:249], v218 offset:27648
	v_cvt_pk_f16_f32 v226, v226, v227
	v_cvt_pk_f16_f32 v227, v228, v229
	v_cvt_pk_f16_f32 v228, v230, v231
	v_cvt_pk_f16_f32 v229, v232, v233
	v_pk_max_f16 v226, v226, 0
	v_pk_max_f16 v227, v227, 0
	v_pk_max_f16 v228, v228, 0
	v_pk_max_f16 v229, v229, 0
	s_waitcnt lgkmcnt(12)
	v_mfma_f32_32x32x16_f16 v[98:113], v[250:253], v[138:141], v[98:113]
	ds_read_b128 v[250:253], v218 offset:28672
	v_cvt_pk_f16_f32 v230, v234, v235
	v_cvt_pk_f16_f32 v231, v236, v237
	v_cvt_pk_f16_f32 v232, v238, v239
	v_cvt_pk_f16_f32 v233, v240, v241
	v_pk_max_f16 v230, v230, 0
	v_pk_max_f16 v231, v231, 0
	v_pk_max_f16 v232, v232, 0
	v_pk_max_f16 v233, v233, 0
	s_waitcnt lgkmcnt(8)
	v_mfma_f32_32x32x16_f16 v[66:81], v[150:153], v[126:129], v[66:81]
	ds_read_b128 v[150:153], v218 offset:29696
	s_waitcnt lgkmcnt(4)
	v_mfma_f32_32x32x16_f16 v[66:81], v[154:157], v[130:133], v[66:81]
	ds_read_b128 v[154:157], v218 offset:30720
	s_waitcnt lgkmcnt(4)
	v_mfma_f32_32x32x16_f16 v[66:81], v[242:245], v[134:137], v[66:81]
	ds_read_b128 v[242:245], v218 offset:31744
	v_cvt_pk_f16_f32 v98, v98, v99
	v_cvt_pk_f16_f32 v99, v100, v101
	v_cvt_pk_f16_f32 v100, v102, v103
	v_cvt_pk_f16_f32 v101, v104, v105
	v_pk_max_f16 v98, v98, 0
	v_pk_max_f16 v99, v99, 0
	v_pk_max_f16 v100, v100, 0
	v_pk_max_f16 v101, v101, 0
	s_waitcnt lgkmcnt(4)
	v_mfma_f32_32x32x16_f16 v[66:81], v[246:249], v[138:141], v[66:81]
	ds_read_b128 v[246:249], v218 offset:32768
	v_cvt_pk_f16_f32 v102, v106, v107
	v_cvt_pk_f16_f32 v103, v108, v109
	v_cvt_pk_f16_f32 v104, v110, v111
	v_cvt_pk_f16_f32 v105, v112, v113
	v_pk_max_f16 v102, v102, 0
	v_pk_max_f16 v103, v103, 0
	v_pk_max_f16 v104, v104, 0
	v_pk_max_f16 v105, v105, 0
	s_waitcnt lgkmcnt(4)
	v_mfma_f32_32x32x16_f16 v[82:97], v[250:253], v[126:129], v[82:97]
	ds_read_b128 v[250:253], v218 offset:33792
	s_waitcnt lgkmcnt(4)
	v_mfma_f32_32x32x16_f16 v[82:97], v[150:153], v[130:133], v[82:97]
	ds_read_b128 v[150:153], v218 offset:34816
	s_waitcnt lgkmcnt(4)
	v_mfma_f32_32x32x16_f16 v[82:97], v[154:157], v[134:137], v[82:97]
	ds_read_b128 v[154:157], v218 offset:35840
	v_cvt_pk_f16_f32 v66, v66, v67
	v_cvt_pk_f16_f32 v67, v68, v69
	v_cvt_pk_f16_f32 v68, v70, v71
	v_cvt_pk_f16_f32 v69, v72, v73
	v_pk_max_f16 v66, v66, 0
	v_pk_max_f16 v67, v67, 0
	v_pk_max_f16 v68, v68, 0
	v_pk_max_f16 v69, v69, 0
	s_waitcnt lgkmcnt(4)
	v_mfma_f32_32x32x16_f16 v[82:97], v[242:245], v[138:141], v[82:97]
	ds_read_b128 v[242:245], v218 offset:36864
	v_cvt_pk_f16_f32 v70, v74, v75
	v_cvt_pk_f16_f32 v71, v76, v77
	v_cvt_pk_f16_f32 v72, v78, v79
	v_cvt_pk_f16_f32 v73, v80, v81
	v_pk_max_f16 v70, v70, 0
	v_pk_max_f16 v71, v71, 0
	v_pk_max_f16 v72, v72, 0
	v_pk_max_f16 v73, v73, 0
	s_waitcnt lgkmcnt(4)
	v_mfma_f32_32x32x16_f16 v[126:141], v[246:249], v[226:229], v[2:17]
	ds_read_b128 v[246:249], v218 offset:37888
	s_waitcnt lgkmcnt(4)
	v_mfma_f32_32x32x16_f16 v[126:141], v[250:253], v[230:233], v[126:141]
	ds_read_b128 v[250:253], v218 offset:38912
	s_waitcnt lgkmcnt(4)
	v_mfma_f32_32x32x16_f16 v[126:141], v[150:153], v[98:101], v[126:141]
	ds_read_b128 v[150:153], v218 offset:39936
	s_waitcnt lgkmcnt(4)
	v_mfma_f32_32x32x16_f16 v[126:141], v[154:157], v[102:105], v[126:141]
	ds_read_b128 v[154:157], v218 offset:40960
	s_waitcnt lgkmcnt(4)
	v_mfma_f32_32x32x16_f16 v[126:141], v[242:245], v[66:69], v[126:141]
	ds_read_b128 v[242:245], v218 offset:41984
	v_cvt_pk_f16_f32 v97, v96, v97
	v_cvt_pk_f16_f32 v96, v94, v95
	v_cvt_pk_f16_f32 v95, v92, v93
	v_cvt_pk_f16_f32 v94, v90, v91
	v_pk_max_f16 v97, v97, 0
	v_pk_max_f16 v96, v96, 0
	v_pk_max_f16 v95, v95, 0
	v_pk_max_f16 v94, v94, 0
	s_waitcnt lgkmcnt(4)
	v_mfma_f32_32x32x16_f16 v[126:141], v[246:249], v[70:73], v[126:141]
	ds_read_b128 v[246:249], v218 offset:43008
	v_cvt_pk_f16_f32 v93, v88, v89
	v_cvt_pk_f16_f32 v92, v86, v87
	v_cvt_pk_f16_f32 v91, v84, v85
	v_cvt_pk_f16_f32 v90, v82, v83
	v_pk_max_f16 v93, v93, 0
	v_pk_max_f16 v92, v92, 0
	v_pk_max_f16 v91, v91, 0
	v_pk_max_f16 v90, v90, 0
	s_waitcnt lgkmcnt(4)
	s_nop 0
	v_mfma_f32_32x32x16_f16 v[126:141], v[250:253], v[90:93], v[126:141]
	ds_read_b128 v[250:253], v218 offset:44032
	s_waitcnt lgkmcnt(4)
	v_mfma_f32_32x32x16_f16 v[126:141], v[150:153], v[94:97], v[126:141]
	ds_read_b128 v[150:153], v218 offset:45056
	s_waitcnt lgkmcnt(4)
	v_mfma_f32_32x32x16_f16 v[74:89], v[154:157], v[226:229], v[34:49]
	ds_read_b128 v[154:157], v218 offset:46080
	s_waitcnt lgkmcnt(4)
	v_mfma_f32_32x32x16_f16 v[74:89], v[242:245], v[230:233], v[74:89]
	ds_read_b128 v[242:245], v218 offset:47104
	s_waitcnt lgkmcnt(4)
	v_mfma_f32_32x32x16_f16 v[74:89], v[246:249], v[98:101], v[74:89]
	ds_read_b128 v[246:249], v218 offset:48128
	s_waitcnt lgkmcnt(4)
	v_mfma_f32_32x32x16_f16 v[74:89], v[250:253], v[102:105], v[74:89]
	s_waitcnt lgkmcnt(3)
	v_mfma_f32_32x32x16_f16 v[74:89], v[150:153], v[66:69], v[74:89]
	ds_read_b128 v[150:153], v218
	v_max3_f32 v254, v126, v127, v128
	v_max3_f32 v255, v129, v130, v131
	v_max3_f32 v254, v254, v132, v133
	v_max3_f32 v255, v255, v134, v135
	v_max3_f32 v254, v254, v136, v137
	v_max3_f32 v255, v255, v138, v139
	v_max3_f32 v254, v254, v140, v141
	v_max_f32_e32 v254, v254, v255
	v_cmp_lt_f32_e32 vcc, s5, v254
	s_cbranch_vccz .Lm_norescale0
	v_max_f32_e32 v234, 0, v126
	v_max_f32_e32 v235, 0, v127
	v_max_f32_e32 v236, 0, v128
	v_max_f32_e32 v237, 0, v129
	v_max_f32_e32 v238, 0, v130
	v_max_f32_e32 v239, 0, v131
	v_max_f32_e32 v240, 0, v132
	v_max_f32_e32 v241, 0, v133
	v_max_f32_e32 v106, 0, v134
	v_max_f32_e32 v107, 0, v135
	v_max_f32_e32 v108, 0, v136
	v_max_f32_e32 v109, 0, v137
	v_max_f32_e32 v110, 0, v138
	v_max_f32_e32 v111, 0, v139
	v_max_f32_e32 v112, 0, v140
	v_max_f32_e32 v113, 0, v141
	v_sub_f32_e32 v126, v126, v234
	v_sub_f32_e32 v127, v127, v235
	v_sub_f32_e32 v128, v128, v236
	v_sub_f32_e32 v129, v129, v237
	v_sub_f32_e32 v130, v130, v238
	v_sub_f32_e32 v131, v131, v239
	v_sub_f32_e32 v132, v132, v240
	v_sub_f32_e32 v133, v133, v241
	v_sub_f32_e32 v134, v134, v106
	v_sub_f32_e32 v135, v135, v107
	v_sub_f32_e32 v136, v136, v108
	v_sub_f32_e32 v137, v137, v109
	v_sub_f32_e32 v138, v138, v110
	v_sub_f32_e32 v139, v139, v111
	v_sub_f32_e32 v140, v140, v112
	v_sub_f32_e32 v141, v141, v113
	v_sub_f32_e32 v2, v2, v234
	v_sub_f32_e32 v3, v3, v235
	v_sub_f32_e32 v4, v4, v236
	v_sub_f32_e32 v5, v5, v237
	v_sub_f32_e32 v6, v6, v238
	v_sub_f32_e32 v7, v7, v239
	v_sub_f32_e32 v8, v8, v240
	v_sub_f32_e32 v9, v9, v241
	v_sub_f32_e32 v10, v10, v106
	v_sub_f32_e32 v11, v11, v107
	v_sub_f32_e32 v12, v12, v108
	v_sub_f32_e32 v13, v13, v109
	v_sub_f32_e32 v14, v14, v110
	v_sub_f32_e32 v15, v15, v111
	v_sub_f32_e32 v16, v16, v112
	v_sub_f32_e32 v17, v17, v113
	v_exp_f32_e64 v234, -v234
	v_exp_f32_e64 v235, -v235
	v_exp_f32_e64 v236, -v236
	v_exp_f32_e64 v237, -v237
	v_exp_f32_e64 v238, -v238
	v_exp_f32_e64 v239, -v239
	v_exp_f32_e64 v240, -v240
	v_exp_f32_e64 v241, -v241
	v_exp_f32_e64 v106, -v106
	v_exp_f32_e64 v107, -v107
	v_exp_f32_e64 v108, -v108
	v_exp_f32_e64 v109, -v109
	v_exp_f32_e64 v110, -v110
	v_exp_f32_e64 v111, -v111
	v_exp_f32_e64 v112, -v112
	v_exp_f32_e64 v113, -v113
	s_nop 0
	v_mul_f32_e32 v50, v234, v50
	v_mul_f32_e32 v51, v235, v51
	v_mul_f32_e32 v52, v236, v52
	v_mul_f32_e32 v53, v237, v53
	v_mul_f32_e32 v54, v238, v54
	v_mul_f32_e32 v55, v239, v55
	v_mul_f32_e32 v56, v240, v56
	v_mul_f32_e32 v57, v241, v57
	v_mul_f32_e32 v58, v106, v58
	v_mul_f32_e32 v59, v107, v59
	v_mul_f32_e32 v60, v108, v60
	v_mul_f32_e32 v61, v109, v61
	v_mul_f32_e32 v62, v110, v62
	v_mul_f32_e32 v63, v111, v63
	v_mul_f32_e32 v64, v112, v64
	v_mul_f32_e32 v65, v113, v65
	v_mul_f32_e32 v216, v234, v216
	v_mul_f32_e32 v217, v235, v217
	v_mul_f32_e32 v214, v236, v214
	v_mul_f32_e32 v215, v237, v215
	v_mul_f32_e32 v212, v238, v212
	v_mul_f32_e32 v213, v239, v213
	v_mul_f32_e32 v210, v240, v210
	v_mul_f32_e32 v211, v241, v211
	v_mul_f32_e32 v208, v106, v208
	v_mul_f32_e32 v209, v107, v209
	v_mul_f32_e32 v204, v108, v204
	v_mul_f32_e32 v205, v109, v205
	v_mul_f32_e32 v202, v110, v202
	v_mul_f32_e32 v203, v111, v203
	v_mul_f32_e32 v196, v112, v196
	v_mul_f32_e32 v197, v113, v197
	s_nop 1
